# v61 + phase E mid-K gate hook also touches the third gate segment so later hook/epilogue gate loads hit cache
# baseline (speedup 1.0000x reference)
.LBB0_3865:
	v_mov_b32_e32 v130, v246
	s_cmpk_eq_i32 s20, 0x400
	v_add_u32_e32 v130, s50, v130
	s_cselect_b32 s0, 0, 0x800
	v_mul_lo_u32 v130, v130, s64
	v_or_b32_e32 v131, s17, v249
	v_add3_u32 v130, v131, s0, v130
	v_add_u32_e32 v131, 0x18000, v130
	global_load_dwordx4 v[186:189], v130, s[10:11]
	global_load_dwordx4 v[190:193], v130, s[10:11] offset:2048
	global_load_dwordx4 v[178:181], v131, s[10:11]
	global_load_dwordx4 v[182:185], v131, s[10:11] offset:2048
	v_add_u32_e32 v131, 0x30000, v130
	global_load_dwordx4 v[170:173], v131, s[10:11]
	global_load_dwordx4 v[174:177], v131, s[10:11] offset:2048
	v_add_u32_e32 v131, 0x48000, v130
	global_load_dwordx4 v[162:165], v131, s[10:11]
	global_load_dwordx4 v[166:169], v131, s[10:11] offset:2048
	v_add_u32_e32 v131, 0xc0000, v130
	global_load_dwordx4 v[154:157], v131, s[10:11]
	global_load_dwordx4 v[158:161], v131, s[10:11] offset:2048
	v_add_u32_e32 v131, 0xd8000, v130
	global_load_dwordx4 v[146:149], v131, s[10:11]
	global_load_dwordx4 v[150:153], v131, s[10:11] offset:2048
	v_add_u32_e32 v131, 0xf0000, v130
	v_add_u32_e32 v134, 0x108000, v130
	v_add_u32_e32 v203, 0x1000, v130
	global_load_dword v205, v203, s[10:11]
	v_add_u32_e32 v203, 0x19000, v130
	global_load_dword v205, v203, s[10:11]
	v_add_u32_e32 v203, 0x31000, v130
	global_load_dword v205, v203, s[10:11]
	v_add_u32_e32 v203, 0x49000, v130
	global_load_dword v205, v203, s[10:11]
	v_add_u32_e32 v203, 0xc1000, v130
	global_load_dword v205, v203, s[10:11]
	v_add_u32_e32 v203, 0xd9000, v130
	global_load_dword v205, v203, s[10:11]
	v_add_u32_e32 v203, 0xf1000, v130
	global_load_dword v205, v203, s[10:11]
	v_add_u32_e32 v203, 0x109000, v130
	global_load_dword v205, v203, s[10:11]
	global_load_dwordx4 v[138:141], v131, s[10:11]
	global_load_dwordx4 v[142:145], v131, s[10:11] offset:2048
	s_nop 0
	global_load_dwordx4 v[130:133], v134, s[10:11]
	s_nop 0
	global_load_dwordx4 v[134:137], v134, s[10:11] offset:2048
	s_waitcnt vmcnt(0)
	s_nop 0
	v_cvt_f32_ubyte0_e32 v203, v190
	v_cvt_f32_ubyte1_e32 v205, v190
	v_cvt_f32_ubyte2_e32 v207, v190
	v_cvt_f32_ubyte3_e32 v213, v190
	v_cvt_f32_ubyte0_e32 v214, v191
	v_cvt_f32_ubyte1_e32 v215, v191
	v_cvt_f32_ubyte2_e32 v223, v191
	v_cvt_f32_ubyte3_e32 v225, v191
	v_rcp_iflag_f32_e32 v190, v203
	v_rcp_iflag_f32_e32 v191, v205
	v_rcp_iflag_f32_e32 v212, v207
	v_rcp_iflag_f32_e32 v213, v213
	v_rcp_iflag_f32_e32 v214, v214
	v_rcp_iflag_f32_e32 v215, v215
	v_rcp_iflag_f32_e32 v224, v223
	v_rcp_iflag_f32_e32 v225, v225
	v_cvt_f32_ubyte3_e32 v227, v186
	v_cvt_f32_ubyte2_e32 v226, v186
	v_cvt_f32_ubyte1_e32 v231, v186
	v_cvt_f32_ubyte0_e32 v230, v186
	v_pk_mul_f32 v[190:191], v[190:191], v[230:231]
	v_pk_mul_f32 v[212:213], v[212:213], v[226:227]
	v_pk_mul_f32 v[126:127], v[126:127], v[190:191]
	v_pk_mul_f32 v[128:129], v[128:129], v[212:213]
	v_cvt_f32_ubyte3_e32 v191, v187
	v_cvt_f32_ubyte2_e32 v190, v187
	v_cvt_f32_ubyte1_e32 v213, v187
	v_cvt_f32_ubyte0_e32 v212, v187
	v_pk_mul_f32 v[186:187], v[214:215], v[212:213]
	v_pk_mul_f32 v[190:191], v[224:225], v[190:191]
	v_pk_mul_f32 v[122:123], v[122:123], v[186:187]
	v_pk_mul_f32 v[124:125], v[124:125], v[190:191]
	v_cvt_f32_ubyte0_e32 v186, v192
	v_cvt_f32_ubyte1_e32 v187, v192
	v_cvt_f32_ubyte2_e32 v190, v192
	v_cvt_f32_ubyte3_e32 v191, v192
	v_rcp_iflag_f32_e32 v186, v186
	v_rcp_iflag_f32_e32 v187, v187
	v_rcp_iflag_f32_e32 v190, v190
	v_rcp_iflag_f32_e32 v191, v191
	v_cvt_f32_ubyte0_e32 v192, v193
	v_cvt_f32_ubyte1_e32 v203, v193
	v_cvt_f32_ubyte2_e32 v205, v193
	v_cvt_f32_ubyte3_e32 v207, v193
	v_rcp_iflag_f32_e32 v192, v192
	v_rcp_iflag_f32_e32 v193, v203
	v_rcp_iflag_f32_e32 v212, v205
	v_rcp_iflag_f32_e32 v213, v207
	v_cvt_f32_ubyte3_e32 v215, v188
	v_cvt_f32_ubyte2_e32 v214, v188
	v_cvt_f32_ubyte1_e32 v225, v188
	v_cvt_f32_ubyte0_e32 v224, v188
	v_pk_mul_f32 v[186:187], v[186:187], v[224:225]
	v_pk_mul_f32 v[190:191], v[190:191], v[214:215]
	v_pk_mul_f32 v[118:119], v[118:119], v[186:187]
	v_pk_mul_f32 v[120:121], v[120:121], v[190:191]
	v_cvt_f32_ubyte3_e32 v187, v189
	v_cvt_f32_ubyte2_e32 v186, v189
	v_cvt_f32_ubyte1_e32 v191, v189
	v_cvt_f32_ubyte0_e32 v190, v189
	v_pk_mul_f32 v[188:189], v[192:193], v[190:191]
	v_pk_mul_f32 v[186:187], v[212:213], v[186:187]
	v_pk_mul_f32 v[114:115], v[114:115], v[188:189]
	v_pk_mul_f32 v[116:117], v[116:117], v[186:187]
	v_cvt_f32_ubyte0_e32 v186, v182
	v_cvt_f32_ubyte1_e32 v187, v182
	v_cvt_f32_ubyte2_e32 v188, v182
	v_cvt_f32_ubyte3_e32 v189, v182
	v_cvt_f32_ubyte0_e32 v190, v183
	v_cvt_f32_ubyte1_e32 v191, v183
	v_cvt_f32_ubyte2_e32 v192, v183
	v_cvt_f32_ubyte3_e32 v193, v183
	v_rcp_iflag_f32_e32 v182, v186
	v_rcp_iflag_f32_e32 v183, v187
	v_rcp_iflag_f32_e32 v186, v188
	v_rcp_iflag_f32_e32 v187, v189
	v_rcp_iflag_f32_e32 v188, v190
	v_rcp_iflag_f32_e32 v189, v191
	v_rcp_iflag_f32_e32 v190, v192
	v_rcp_iflag_f32_e32 v191, v193
	v_cvt_f32_ubyte3_e32 v193, v178
	v_cvt_f32_ubyte2_e32 v192, v178
	v_cvt_f32_ubyte1_e32 v213, v178
	v_cvt_f32_ubyte0_e32 v212, v178
	v_pk_mul_f32 v[182:183], v[182:183], v[212:213]
	v_pk_mul_f32 v[186:187], v[186:187], v[192:193]
	v_pk_mul_f32 v[110:111], v[110:111], v[182:183]
	v_pk_mul_f32 v[112:113], v[112:113], v[186:187]
	v_cvt_f32_ubyte3_e32 v183, v179
	v_cvt_f32_ubyte2_e32 v182, v179
	v_cvt_f32_ubyte1_e32 v187, v179
	v_cvt_f32_ubyte0_e32 v186, v179
	v_pk_mul_f32 v[178:179], v[188:189], v[186:187]
	v_pk_mul_f32 v[182:183], v[190:191], v[182:183]
	v_pk_mul_f32 v[106:107], v[106:107], v[178:179]
	v_pk_mul_f32 v[108:109], v[108:109], v[182:183]
	v_cvt_f32_ubyte0_e32 v178, v184
	v_cvt_f32_ubyte1_e32 v179, v184
	v_cvt_f32_ubyte2_e32 v182, v184
	v_cvt_f32_ubyte3_e32 v183, v184
	v_rcp_iflag_f32_e32 v178, v178
	v_rcp_iflag_f32_e32 v179, v179
	v_rcp_iflag_f32_e32 v182, v182
	v_rcp_iflag_f32_e32 v183, v183
	v_cvt_f32_ubyte0_e32 v184, v185
	v_cvt_f32_ubyte1_e32 v186, v185
	v_cvt_f32_ubyte2_e32 v187, v185
	v_cvt_f32_ubyte3_e32 v188, v185
	v_rcp_iflag_f32_e32 v184, v184
	v_rcp_iflag_f32_e32 v185, v186
	v_rcp_iflag_f32_e32 v186, v187
	v_rcp_iflag_f32_e32 v187, v188
	v_cvt_f32_ubyte3_e32 v189, v180
	v_cvt_f32_ubyte2_e32 v188, v180
	v_cvt_f32_ubyte1_e32 v191, v180
	v_cvt_f32_ubyte0_e32 v190, v180
	v_pk_mul_f32 v[178:179], v[178:179], v[190:191]
	v_pk_mul_f32 v[182:183], v[182:183], v[188:189]
	v_pk_mul_f32 v[102:103], v[102:103], v[178:179]
	v_pk_mul_f32 v[104:105], v[104:105], v[182:183]
	v_cvt_f32_ubyte3_e32 v179, v181
	v_cvt_f32_ubyte2_e32 v178, v181
	v_cvt_f32_ubyte1_e32 v183, v181
	v_cvt_f32_ubyte0_e32 v182, v181
	v_pk_mul_f32 v[180:181], v[184:185], v[182:183]
	v_pk_mul_f32 v[178:179], v[186:187], v[178:179]
	v_pk_mul_f32 v[98:99], v[98:99], v[180:181]
	v_pk_mul_f32 v[100:101], v[100:101], v[178:179]
	v_cvt_f32_ubyte0_e32 v178, v174
	v_cvt_f32_ubyte1_e32 v179, v174
	v_cvt_f32_ubyte2_e32 v180, v174
	v_cvt_f32_ubyte3_e32 v181, v174
	v_cvt_f32_ubyte0_e32 v182, v175
	v_cvt_f32_ubyte1_e32 v183, v175
	v_cvt_f32_ubyte2_e32 v184, v175
	v_cvt_f32_ubyte3_e32 v185, v175
	v_rcp_iflag_f32_e32 v174, v178
	v_rcp_iflag_f32_e32 v175, v179
	v_rcp_iflag_f32_e32 v178, v180
	v_rcp_iflag_f32_e32 v179, v181
	v_rcp_iflag_f32_e32 v180, v182
	v_rcp_iflag_f32_e32 v181, v183
	v_rcp_iflag_f32_e32 v182, v184
	v_rcp_iflag_f32_e32 v183, v185
	v_cvt_f32_ubyte3_e32 v185, v170
	v_cvt_f32_ubyte2_e32 v184, v170
	v_cvt_f32_ubyte1_e32 v187, v170
	v_cvt_f32_ubyte0_e32 v186, v170
	v_pk_mul_f32 v[174:175], v[174:175], v[186:187]
	v_pk_mul_f32 v[178:179], v[178:179], v[184:185]
	v_pk_mul_f32 v[94:95], v[94:95], v[174:175]
	v_pk_mul_f32 v[96:97], v[96:97], v[178:179]
	v_cvt_f32_ubyte3_e32 v175, v171
	v_cvt_f32_ubyte2_e32 v174, v171
	v_cvt_f32_ubyte1_e32 v179, v171
	v_cvt_f32_ubyte0_e32 v178, v171
	v_pk_mul_f32 v[170:171], v[180:181], v[178:179]
	v_pk_mul_f32 v[174:175], v[182:183], v[174:175]
	v_pk_mul_f32 v[90:91], v[90:91], v[170:171]
	v_pk_mul_f32 v[92:93], v[92:93], v[174:175]
	v_cvt_f32_ubyte0_e32 v170, v176
	v_cvt_f32_ubyte1_e32 v171, v176
	v_cvt_f32_ubyte2_e32 v174, v176
	v_cvt_f32_ubyte3_e32 v175, v176
	v_rcp_iflag_f32_e32 v170, v170
	v_rcp_iflag_f32_e32 v171, v171
	v_rcp_iflag_f32_e32 v174, v174
	v_rcp_iflag_f32_e32 v175, v175
	v_cvt_f32_ubyte0_e32 v176, v177
	v_cvt_f32_ubyte1_e32 v178, v177
	v_cvt_f32_ubyte2_e32 v179, v177
	v_cvt_f32_ubyte3_e32 v180, v177
	v_rcp_iflag_f32_e32 v176, v176
	v_rcp_iflag_f32_e32 v177, v178
	v_rcp_iflag_f32_e32 v178, v179
	v_rcp_iflag_f32_e32 v179, v180
	v_cvt_f32_ubyte3_e32 v181, v172
	v_cvt_f32_ubyte2_e32 v180, v172
	v_cvt_f32_ubyte1_e32 v183, v172
	v_cvt_f32_ubyte0_e32 v182, v172
	v_pk_mul_f32 v[170:171], v[170:171], v[182:183]
	v_pk_mul_f32 v[174:175], v[174:175], v[180:181]
	v_pk_mul_f32 v[86:87], v[86:87], v[170:171]
	v_pk_mul_f32 v[88:89], v[88:89], v[174:175]
	v_cvt_f32_ubyte3_e32 v171, v173
	v_cvt_f32_ubyte2_e32 v170, v173
	v_cvt_f32_ubyte1_e32 v175, v173
	v_cvt_f32_ubyte0_e32 v174, v173
	v_pk_mul_f32 v[172:173], v[176:177], v[174:175]
	v_pk_mul_f32 v[170:171], v[178:179], v[170:171]
	v_pk_mul_f32 v[82:83], v[82:83], v[172:173]
	v_pk_mul_f32 v[84:85], v[84:85], v[170:171]
	v_cvt_f32_ubyte0_e32 v170, v166
	v_cvt_f32_ubyte1_e32 v171, v166
	v_cvt_f32_ubyte2_e32 v172, v166
	v_cvt_f32_ubyte3_e32 v173, v166
	v_cvt_f32_ubyte0_e32 v174, v167
	v_cvt_f32_ubyte1_e32 v175, v167
	v_cvt_f32_ubyte2_e32 v176, v167
	v_cvt_f32_ubyte3_e32 v177, v167
	v_rcp_iflag_f32_e32 v166, v170
	v_rcp_iflag_f32_e32 v167, v171
	v_rcp_iflag_f32_e32 v170, v172
	v_rcp_iflag_f32_e32 v171, v173
	v_rcp_iflag_f32_e32 v172, v174
	v_rcp_iflag_f32_e32 v173, v175
	v_rcp_iflag_f32_e32 v174, v176
	v_rcp_iflag_f32_e32 v175, v177
	v_cvt_f32_ubyte3_e32 v177, v162
	v_cvt_f32_ubyte2_e32 v176, v162
	v_cvt_f32_ubyte1_e32 v179, v162
	v_cvt_f32_ubyte0_e32 v178, v162
	v_pk_mul_f32 v[166:167], v[166:167], v[178:179]
	v_pk_mul_f32 v[170:171], v[170:171], v[176:177]
	v_pk_mul_f32 v[78:79], v[78:79], v[166:167]
	v_pk_mul_f32 v[80:81], v[80:81], v[170:171]
	v_cvt_f32_ubyte3_e32 v167, v163
	v_cvt_f32_ubyte2_e32 v166, v163
	v_cvt_f32_ubyte1_e32 v171, v163
	v_cvt_f32_ubyte0_e32 v170, v163
	v_pk_mul_f32 v[162:163], v[172:173], v[170:171]
	v_pk_mul_f32 v[166:167], v[174:175], v[166:167]
	v_pk_mul_f32 v[74:75], v[74:75], v[162:163]
	v_pk_mul_f32 v[76:77], v[76:77], v[166:167]
	v_cvt_f32_ubyte0_e32 v162, v168
	v_cvt_f32_ubyte1_e32 v163, v168
	v_cvt_f32_ubyte2_e32 v166, v168
	v_cvt_f32_ubyte3_e32 v167, v168
	v_rcp_iflag_f32_e32 v162, v162
	v_rcp_iflag_f32_e32 v163, v163
	v_rcp_iflag_f32_e32 v166, v166
	v_rcp_iflag_f32_e32 v167, v167
	v_cvt_f32_ubyte0_e32 v168, v169
	v_cvt_f32_ubyte1_e32 v170, v169
	v_cvt_f32_ubyte2_e32 v171, v169
	v_cvt_f32_ubyte3_e32 v172, v169
	v_rcp_iflag_f32_e32 v168, v168
	v_rcp_iflag_f32_e32 v169, v170
	v_rcp_iflag_f32_e32 v170, v171
	v_rcp_iflag_f32_e32 v171, v172
	v_cvt_f32_ubyte3_e32 v173, v164
	v_cvt_f32_ubyte2_e32 v172, v164
	v_cvt_f32_ubyte1_e32 v175, v164
	v_cvt_f32_ubyte0_e32 v174, v164
	v_pk_mul_f32 v[162:163], v[162:163], v[174:175]
	v_pk_mul_f32 v[166:167], v[166:167], v[172:173]
	v_pk_mul_f32 v[70:71], v[70:71], v[162:163]
	v_pk_mul_f32 v[72:73], v[72:73], v[166:167]
	v_cvt_f32_ubyte3_e32 v163, v165
	v_cvt_f32_ubyte2_e32 v162, v165
	v_cvt_f32_ubyte1_e32 v167, v165
	v_cvt_f32_ubyte0_e32 v166, v165
	v_pk_mul_f32 v[164:165], v[168:169], v[166:167]
	v_pk_mul_f32 v[162:163], v[170:171], v[162:163]
	v_pk_mul_f32 v[66:67], v[66:67], v[164:165]
	v_pk_mul_f32 v[68:69], v[68:69], v[162:163]
	v_cvt_f32_ubyte0_e32 v162, v158
	v_cvt_f32_ubyte1_e32 v163, v158
	v_cvt_f32_ubyte2_e32 v164, v158
	v_cvt_f32_ubyte3_e32 v165, v158
	v_cvt_f32_ubyte0_e32 v166, v159
	v_cvt_f32_ubyte1_e32 v167, v159
	v_cvt_f32_ubyte2_e32 v168, v159
	v_cvt_f32_ubyte3_e32 v169, v159
	v_rcp_iflag_f32_e32 v158, v162
	v_rcp_iflag_f32_e32 v159, v163
	v_rcp_iflag_f32_e32 v162, v164
	v_rcp_iflag_f32_e32 v163, v165
	v_rcp_iflag_f32_e32 v164, v166
	v_rcp_iflag_f32_e32 v165, v167
	v_rcp_iflag_f32_e32 v166, v168
	v_rcp_iflag_f32_e32 v167, v169
	v_cvt_f32_ubyte3_e32 v169, v154
	v_cvt_f32_ubyte2_e32 v168, v154
	v_cvt_f32_ubyte1_e32 v171, v154
	v_cvt_f32_ubyte0_e32 v170, v154
	v_pk_mul_f32 v[158:159], v[158:159], v[170:171]
	v_pk_mul_f32 v[162:163], v[162:163], v[168:169]
	v_pk_mul_f32 v[62:63], v[62:63], v[158:159]
	v_pk_mul_f32 v[64:65], v[64:65], v[162:163]
	v_cvt_f32_ubyte3_e32 v159, v155
	v_cvt_f32_ubyte2_e32 v158, v155
	v_cvt_f32_ubyte1_e32 v163, v155
	v_cvt_f32_ubyte0_e32 v162, v155
	v_pk_mul_f32 v[154:155], v[164:165], v[162:163]
	v_pk_mul_f32 v[158:159], v[166:167], v[158:159]
	v_pk_mul_f32 v[58:59], v[58:59], v[154:155]
	v_pk_mul_f32 v[60:61], v[60:61], v[158:159]
	v_cvt_f32_ubyte0_e32 v154, v160
	v_cvt_f32_ubyte1_e32 v155, v160
	v_cvt_f32_ubyte2_e32 v158, v160
	v_cvt_f32_ubyte3_e32 v159, v160
	v_rcp_iflag_f32_e32 v154, v154
	v_rcp_iflag_f32_e32 v155, v155
	v_rcp_iflag_f32_e32 v158, v158
	v_rcp_iflag_f32_e32 v159, v159
	v_cvt_f32_ubyte0_e32 v160, v161
	v_cvt_f32_ubyte1_e32 v162, v161
	v_cvt_f32_ubyte2_e32 v163, v161
	v_cvt_f32_ubyte3_e32 v164, v161
	v_rcp_iflag_f32_e32 v160, v160
	v_rcp_iflag_f32_e32 v161, v162
	v_rcp_iflag_f32_e32 v162, v163
	v_rcp_iflag_f32_e32 v163, v164
	v_cvt_f32_ubyte3_e32 v165, v156
	v_cvt_f32_ubyte2_e32 v164, v156
	v_cvt_f32_ubyte1_e32 v167, v156
	v_cvt_f32_ubyte0_e32 v166, v156
	v_pk_mul_f32 v[154:155], v[154:155], v[166:167]
	v_pk_mul_f32 v[158:159], v[158:159], v[164:165]
	v_pk_mul_f32 v[54:55], v[54:55], v[154:155]
	v_pk_mul_f32 v[56:57], v[56:57], v[158:159]
	v_cvt_f32_ubyte3_e32 v155, v157
	v_cvt_f32_ubyte2_e32 v154, v157
	v_cvt_f32_ubyte1_e32 v159, v157
	v_cvt_f32_ubyte0_e32 v158, v157
	v_pk_mul_f32 v[156:157], v[160:161], v[158:159]
	v_pk_mul_f32 v[154:155], v[162:163], v[154:155]
	v_pk_mul_f32 v[50:51], v[50:51], v[156:157]
	v_pk_mul_f32 v[52:53], v[52:53], v[154:155]
	v_cvt_f32_ubyte0_e32 v154, v150
	v_cvt_f32_ubyte1_e32 v155, v150
	v_cvt_f32_ubyte2_e32 v156, v150
	v_cvt_f32_ubyte3_e32 v157, v150
	v_cvt_f32_ubyte0_e32 v158, v151
	v_cvt_f32_ubyte1_e32 v159, v151
	v_cvt_f32_ubyte2_e32 v160, v151
	v_cvt_f32_ubyte3_e32 v161, v151
	v_rcp_iflag_f32_e32 v150, v154
	v_rcp_iflag_f32_e32 v151, v155
	v_rcp_iflag_f32_e32 v154, v156
	v_rcp_iflag_f32_e32 v155, v157
	v_rcp_iflag_f32_e32 v156, v158
	v_rcp_iflag_f32_e32 v157, v159
	v_rcp_iflag_f32_e32 v158, v160
	v_rcp_iflag_f32_e32 v159, v161
	v_cvt_f32_ubyte3_e32 v161, v146
	v_cvt_f32_ubyte2_e32 v160, v146
	v_cvt_f32_ubyte1_e32 v163, v146
	v_cvt_f32_ubyte0_e32 v162, v146
	v_pk_mul_f32 v[150:151], v[150:151], v[162:163]
	v_pk_mul_f32 v[154:155], v[154:155], v[160:161]
	v_pk_mul_f32 v[46:47], v[46:47], v[150:151]
	v_pk_mul_f32 v[48:49], v[48:49], v[154:155]
	v_cvt_f32_ubyte3_e32 v151, v147
	v_cvt_f32_ubyte2_e32 v150, v147
	v_cvt_f32_ubyte1_e32 v155, v147
	v_cvt_f32_ubyte0_e32 v154, v147
	v_pk_mul_f32 v[146:147], v[156:157], v[154:155]
	v_pk_mul_f32 v[150:151], v[158:159], v[150:151]
	v_pk_mul_f32 v[42:43], v[42:43], v[146:147]
	v_pk_mul_f32 v[44:45], v[44:45], v[150:151]
	v_cvt_f32_ubyte0_e32 v146, v152
	v_cvt_f32_ubyte1_e32 v147, v152
	v_cvt_f32_ubyte2_e32 v150, v152
	v_cvt_f32_ubyte3_e32 v151, v152
	v_rcp_iflag_f32_e32 v146, v146
	v_rcp_iflag_f32_e32 v147, v147
	v_rcp_iflag_f32_e32 v150, v150
	v_rcp_iflag_f32_e32 v151, v151
	v_cvt_f32_ubyte0_e32 v152, v153
	v_cvt_f32_ubyte1_e32 v154, v153
	v_cvt_f32_ubyte2_e32 v155, v153
	v_cvt_f32_ubyte3_e32 v156, v153
	v_rcp_iflag_f32_e32 v152, v152
	v_rcp_iflag_f32_e32 v153, v154
	v_rcp_iflag_f32_e32 v154, v155
	v_rcp_iflag_f32_e32 v155, v156
	v_cvt_f32_ubyte3_e32 v157, v148
	v_cvt_f32_ubyte2_e32 v156, v148
	v_cvt_f32_ubyte1_e32 v159, v148
	v_cvt_f32_ubyte0_e32 v158, v148
	v_pk_mul_f32 v[146:147], v[146:147], v[158:159]
	v_pk_mul_f32 v[150:151], v[150:151], v[156:157]
	v_pk_mul_f32 v[38:39], v[38:39], v[146:147]
	v_pk_mul_f32 v[40:41], v[40:41], v[150:151]
	v_cvt_f32_ubyte3_e32 v147, v149
	v_cvt_f32_ubyte2_e32 v146, v149
	v_cvt_f32_ubyte1_e32 v151, v149
	v_cvt_f32_ubyte0_e32 v150, v149
	v_pk_mul_f32 v[148:149], v[152:153], v[150:151]
	v_pk_mul_f32 v[146:147], v[154:155], v[146:147]
	v_pk_mul_f32 v[34:35], v[34:35], v[148:149]
	v_pk_mul_f32 v[36:37], v[36:37], v[146:147]
	v_cvt_f32_ubyte0_e32 v146, v142
	v_cvt_f32_ubyte1_e32 v147, v142
	v_cvt_f32_ubyte2_e32 v148, v142
	v_cvt_f32_ubyte3_e32 v149, v142
	v_cvt_f32_ubyte0_e32 v150, v143
	v_cvt_f32_ubyte1_e32 v151, v143
	v_cvt_f32_ubyte2_e32 v152, v143
	v_cvt_f32_ubyte3_e32 v153, v143
	v_rcp_iflag_f32_e32 v142, v146
	v_rcp_iflag_f32_e32 v143, v147
	v_rcp_iflag_f32_e32 v146, v148
	v_rcp_iflag_f32_e32 v147, v149
	v_rcp_iflag_f32_e32 v148, v150
	v_rcp_iflag_f32_e32 v149, v151
	v_rcp_iflag_f32_e32 v150, v152
	v_rcp_iflag_f32_e32 v151, v153
	v_cvt_f32_ubyte3_e32 v153, v138
	v_cvt_f32_ubyte2_e32 v152, v138
	v_cvt_f32_ubyte1_e32 v155, v138
	v_cvt_f32_ubyte0_e32 v154, v138
	v_pk_mul_f32 v[142:143], v[142:143], v[154:155]
	v_pk_mul_f32 v[146:147], v[146:147], v[152:153]
	v_pk_mul_f32 v[30:31], v[30:31], v[142:143]
	v_pk_mul_f32 v[32:33], v[32:33], v[146:147]
	v_cvt_f32_ubyte3_e32 v143, v139
	v_cvt_f32_ubyte2_e32 v142, v139
	v_cvt_f32_ubyte1_e32 v147, v139
	v_cvt_f32_ubyte0_e32 v146, v139
	v_pk_mul_f32 v[138:139], v[148:149], v[146:147]
	v_pk_mul_f32 v[142:143], v[150:151], v[142:143]
	v_pk_mul_f32 v[26:27], v[26:27], v[138:139]
	v_pk_mul_f32 v[28:29], v[28:29], v[142:143]
	v_cvt_f32_ubyte0_e32 v138, v144
	v_cvt_f32_ubyte1_e32 v139, v144
	v_cvt_f32_ubyte2_e32 v142, v144
	v_cvt_f32_ubyte3_e32 v143, v144
	v_rcp_iflag_f32_e32 v138, v138
	v_rcp_iflag_f32_e32 v139, v139
	v_rcp_iflag_f32_e32 v142, v142
	v_rcp_iflag_f32_e32 v143, v143
	v_cvt_f32_ubyte0_e32 v144, v145
	v_cvt_f32_ubyte1_e32 v146, v145
	v_cvt_f32_ubyte2_e32 v147, v145
	v_cvt_f32_ubyte3_e32 v148, v145
	v_rcp_iflag_f32_e32 v144, v144
	v_rcp_iflag_f32_e32 v145, v146
	v_rcp_iflag_f32_e32 v146, v147
	v_rcp_iflag_f32_e32 v147, v148
	v_cvt_f32_ubyte3_e32 v149, v140
	v_cvt_f32_ubyte2_e32 v148, v140
	v_cvt_f32_ubyte1_e32 v151, v140
	v_cvt_f32_ubyte0_e32 v150, v140
	v_pk_mul_f32 v[138:139], v[138:139], v[150:151]
	v_pk_mul_f32 v[142:143], v[142:143], v[148:149]
	v_pk_mul_f32 v[22:23], v[22:23], v[138:139]
	v_pk_mul_f32 v[24:25], v[24:25], v[142:143]
	v_cvt_f32_ubyte3_e32 v139, v141
	v_cvt_f32_ubyte2_e32 v138, v141
	v_cvt_f32_ubyte1_e32 v143, v141
	v_cvt_f32_ubyte0_e32 v142, v141
	v_pk_mul_f32 v[140:141], v[144:145], v[142:143]
	v_pk_mul_f32 v[138:139], v[146:147], v[138:139]
	v_pk_mul_f32 v[18:19], v[18:19], v[140:141]
	v_pk_mul_f32 v[20:21], v[20:21], v[138:139]
	v_cvt_f32_ubyte0_e32 v138, v134
	v_cvt_f32_ubyte1_e32 v139, v134
	v_cvt_f32_ubyte2_e32 v140, v134
	v_cvt_f32_ubyte3_e32 v141, v134
	v_cvt_f32_ubyte0_e32 v142, v135
	v_cvt_f32_ubyte1_e32 v143, v135
	v_cvt_f32_ubyte2_e32 v144, v135
	v_cvt_f32_ubyte3_e32 v145, v135
	v_rcp_iflag_f32_e32 v134, v138
	v_rcp_iflag_f32_e32 v135, v139
	v_rcp_iflag_f32_e32 v138, v140
	v_rcp_iflag_f32_e32 v139, v141
	v_rcp_iflag_f32_e32 v140, v142
	v_rcp_iflag_f32_e32 v141, v143
	v_rcp_iflag_f32_e32 v142, v144
	v_rcp_iflag_f32_e32 v143, v145
	v_cvt_f32_ubyte3_e32 v145, v130
	v_cvt_f32_ubyte2_e32 v144, v130
	v_cvt_f32_ubyte1_e32 v147, v130
	v_cvt_f32_ubyte0_e32 v146, v130
	v_pk_mul_f32 v[134:135], v[134:135], v[146:147]
	v_pk_mul_f32 v[138:139], v[138:139], v[144:145]
	v_pk_mul_f32 v[14:15], v[14:15], v[134:135]
	v_pk_mul_f32 v[16:17], v[16:17], v[138:139]
	v_cvt_f32_ubyte3_e32 v135, v131
	v_cvt_f32_ubyte2_e32 v134, v131
	v_cvt_f32_ubyte1_e32 v139, v131
	v_cvt_f32_ubyte0_e32 v138, v131
	v_pk_mul_f32 v[130:131], v[140:141], v[138:139]
	v_pk_mul_f32 v[134:135], v[142:143], v[134:135]
	v_pk_mul_f32 v[10:11], v[10:11], v[130:131]
	v_pk_mul_f32 v[12:13], v[12:13], v[134:135]
	v_cvt_f32_ubyte0_e32 v130, v136
	v_cvt_f32_ubyte1_e32 v131, v136
	v_cvt_f32_ubyte2_e32 v134, v136
	v_cvt_f32_ubyte3_e32 v135, v136
	v_rcp_iflag_f32_e32 v130, v130
	v_rcp_iflag_f32_e32 v131, v131
	v_rcp_iflag_f32_e32 v134, v134
	v_rcp_iflag_f32_e32 v135, v135
	v_cvt_f32_ubyte0_e32 v136, v137
	v_cvt_f32_ubyte1_e32 v138, v137
	v_cvt_f32_ubyte2_e32 v139, v137
	v_cvt_f32_ubyte3_e32 v140, v137
	v_rcp_iflag_f32_e32 v136, v136
	v_rcp_iflag_f32_e32 v137, v138
	v_rcp_iflag_f32_e32 v138, v139
	v_rcp_iflag_f32_e32 v139, v140
	v_cvt_f32_ubyte3_e32 v141, v132
	v_cvt_f32_ubyte2_e32 v140, v132
	v_cvt_f32_ubyte1_e32 v143, v132
	v_cvt_f32_ubyte0_e32 v142, v132
	v_pk_mul_f32 v[130:131], v[130:131], v[142:143]
	v_pk_mul_f32 v[134:135], v[134:135], v[140:141]
	v_pk_mul_f32 v[6:7], v[6:7], v[130:131]
	v_pk_mul_f32 v[8:9], v[8:9], v[134:135]
	v_cvt_f32_ubyte3_e32 v131, v133
	v_cvt_f32_ubyte2_e32 v130, v133
	v_cvt_f32_ubyte1_e32 v135, v133
	v_cvt_f32_ubyte0_e32 v134, v133
	v_pk_mul_f32 v[132:133], v[136:137], v[134:135]
	v_pk_mul_f32 v[130:131], v[138:139], v[130:131]
	v_pk_mul_f32 v[2:3], v[2:3], v[132:133]
	v_pk_mul_f32 v[4:5], v[4:5], v[130:131]
